# attention halves: removed hipcc's s_nop pads that only covered uncounted inline-asm ds_reads; permlane pads filled with independent instructions
# speedup vs baseline: 1.0079x; 1.0024x over previous
; template <bool FIRST> DEVI bool partialSM(f32x16& p0, f32x16& p1, float& m_reg, float& alpha) {
;     float pmax = p0[0];
; #pragma unroll
;     for (int r = 1; r < 16; ++r) pmax = fmaxf(pmax, p0[r]);
; #pragma unroll
;     for (int r = 0; r < 16; ++r) pmax = fmaxf(pmax, p1[r]);
;     { auto rr = __builtin_amdgcn_permlane32_swap(__float_as_uint(pmax), __float_as_uint(pmax), false, false);
;       pmax = fmaxf(__uint_as_float(rr[0]), __uint_as_float(rr[1])); }
;     if (FIRST) { m_reg = pmax; alpha = 1.f;
; #pragma unroll
;         for (int r = 0; r < 16; ++r) { p0[r] = __builtin_amdgcn_exp2f(p0[r] - pmax); p1[r] = p1[r] - pmax; }
;         return false;
;     } else if (__builtin_expect(__all(pmax <= ATT_THR), 1)) { alpha = 1.f;
; #pragma unroll
;         for (int r = 0; r < 16; ++r) p0[r] = __builtin_amdgcn_exp2f(p0[r]);
;         return false;
;     } else { const float d = fmaxf(pmax, 0.f); alpha = __builtin_amdgcn_exp2f(-d); m_reg += d;
; #pragma unroll
;         for (int r = 0; r < 16; ++r) { p0[r] = __builtin_amdgcn_exp2f(p0[r] - d); p1[r] = p1[r] - d; }
;         return true;
;     }
; }
; DEVI void finishSM(f32x16& p0, f32x16& p1, float alpha, float& l_reg, bf16x8& pa0, bf16x8& pa1, bf16x8& pa2, bf16x8& pa3) {
; #pragma unroll
;     for (int r = 0; r < 16; ++r) p1[r] = __builtin_amdgcn_exp2f(p1[r]);
;     f32x2 s2 = (f32x2){p0[0], p0[1]} + (f32x2){p1[0], p1[1]};
; #pragma unroll
;     for (int r = 2; r < 16; r += 2) s2 += (f32x2){p0[r], p0[r + 1]} + (f32x2){p1[r], p1[r + 1]};
;     float ps = s2[0] + s2[1];
;     { auto rr = __builtin_amdgcn_permlane32_swap(__float_as_uint(ps), __float_as_uint(ps), false, false);
;       ps = __uint_as_float(rr[0]) + __uint_as_float(rr[1]); }
;     l_reg = l_reg * alpha + ps;
;     ...
;     PK4(p0, 0, pa0); PK4(p0, 8, pa1); PK4(p1, 0, pa2); PK4(p1, 8, pa3);
;     ...
; }
; DEVI void qkt(f32x16& p0, f32x16& p1, const char* Kb, const bf16x8 (&qr)[6], int r32, int hi, const f32x16& cinit) {
; #pragma unroll
;     for (int d0 = 0; d0 < 6; ++d0) { const int cb = (d0 * 16 + hi * 8) * 2;
;         const bf16x8 k0 = *(const bf16x8*)(Kb + KSWZ(r32, cb)), k1 = *(const bf16x8*)(Kb + KSWZ(32 + r32, cb));
;         p0 = __builtin_amdgcn_mfma_f32_32x32x16_bf16(k0, qr[d0], d0 == 0 ? cinit : p0, 0, 0, 0);
;         p1 = __builtin_amdgcn_mfma_f32_32x32x16_bf16(k1, qr[d0], d0 == 0 ? cinit : p1, 0, 0, 0); }
; }
.LBB0_696:
	v_add_u32_e32 v174, s98, v204
	v_exp_f32_e32 v66, v66
	v_exp_f32_e32 v67, v67
	s_waitcnt lgkmcnt(1)
	v_mfma_f32_32x32x16_bf16 v[98:113], v[82:85], v[150:153], v[34:49]
	v_add_u32_e32 v82, s98, v184
	v_add_u32_e32 v83, s98, v185
	ds_read_b128 v[208:211], v82 offset:12288
	ds_read_b128 v[212:215], v82 offset:18432
	ds_read_b128 v[216:219], v83 offset:12288
	ds_read_b128 v[220:223], v83 offset:18432
	v_exp_f32_e32 v68, v68
	v_exp_f32_e32 v69, v69
	v_exp_f32_e32 v70, v70
	v_exp_f32_e32 v71, v71
	s_waitcnt lgkmcnt(4)
	v_mfma_f32_32x32x16_bf16 v[82:97], v[124:127], v[150:153], v[34:49]
	ds_read_b128 v[124:127], v174 offset:12288
	ds_read_b128 v[224:227], v174 offset:18432
	v_exp_f32_e32 v72, v72
	v_exp_f32_e32 v73, v73
	v_exp_f32_e32 v74, v74
	v_exp_f32_e32 v75, v75
	v_exp_f32_e32 v76, v76
	v_exp_f32_e32 v77, v77
	s_waitcnt lgkmcnt(5)
	v_mfma_f32_32x32x16_bf16 v[98:113], v[208:211], v[138:141], v[98:113]
	v_add_u32_e32 v174, s98, v205
	v_exp_f32_e32 v78, v78
	v_exp_f32_e32 v79, v79
	ds_read_b128 v[228:231], v174 offset:12288
	ds_read_b128 v[232:235], v174 offset:18432
	v_exp_f32_e32 v80, v80
	v_exp_f32_e32 v81, v81
	v_add_u32_e32 v174, s98, v206
	s_waitcnt lgkmcnt(6)
	v_mfma_f32_32x32x16_bf16 v[82:97], v[212:215], v[138:141], v[82:97]
	v_add_f32_e64 v212, v50, v66
	v_add_f32_e64 v213, v51, v67
	v_add_f32_e64 v214, v52, v68
	v_add_f32_e64 v215, v53, v69
	v_lshl_add_u32 v202, s89, 14, v115
	v_add_f32_e32 v212, v214, v212
	v_add_f32_e32 v213, v215, v213
	v_add_f32_e32 v214, v54, v70
	v_add_f32_e32 v215, v55, v71
	ds_read_b128 v[208:211], v174 offset:12288
	ds_read_b128 v[236:239], v174 offset:18432
	v_add_f32_e32 v212, v214, v212
	v_add_f32_e32 v213, v215, v213
	s_waitcnt lgkmcnt(7)
	v_mfma_f32_32x32x16_bf16 v[98:113], v[216:219], v[134:137], v[98:113]
	v_add_f32_e64 v214, v56, v72
	v_add_f32_e64 v215, v57, v73
	v_cvt_pk_bf16_f32 v50, v50, v51
	v_cvt_pk_bf16_f32 v51, v52, v53
	v_cvt_pk_bf16_f32 v52, v54, v55
	v_cvt_pk_bf16_f32 v53, v56, v57
	v_cvt_pk_bf16_f32 v54, v58, v59
	v_add_f32_e64 v212, v214, v212
	v_add_f32_e64 v213, v215, v213
	s_waitcnt lgkmcnt(6)
	v_mfma_f32_32x32x16_bf16 v[82:97], v[220:223], v[134:137], v[82:97]
	v_add_f32_e64 v214, v58, v74
	v_add_f32_e64 v215, v59, v75
	v_cvt_pk_bf16_f32 v55, v60, v61
	v_cvt_pk_bf16_f32 v56, v62, v63
	v_cvt_pk_bf16_f32 v57, v64, v65
	v_cvt_pk_bf16_f32 v58, v66, v67
	v_cvt_pk_bf16_f32 v59, v68, v69
	v_add_f32_e64 v212, v214, v212
	v_add_f32_e64 v213, v215, v213
	s_waitcnt lgkmcnt(5)
	v_mfma_f32_32x32x16_bf16 v[98:113], v[124:127], v[130:133], v[98:113]
	v_add_f32_e64 v214, v60, v76
	v_add_f32_e64 v215, v61, v77
	v_add_f32_e64 v126, v62, v78
	v_add_f32_e64 v127, v63, v79
	v_add_f32_e64 v124, v214, v212
	v_add_f32_e64 v125, v215, v213
	v_cvt_pk_bf16_f32 v60, v70, v71
	v_cvt_pk_bf16_f32 v61, v72, v73
	v_cvt_pk_bf16_f32 v62, v74, v75
	v_cvt_pk_bf16_f32 v63, v76, v77
	s_waitcnt lgkmcnt(4)
	v_mfma_f32_32x32x16_bf16 v[82:97], v[224:227], v[130:133], v[82:97]
	v_add_f32_e64 v124, v126, v124
	v_add_f32_e64 v125, v127, v125
	v_add_f32_e64 v126, v64, v80
	v_add_f32_e64 v127, v65, v81
	v_cvt_pk_bf16_f32 v64, v78, v79
	v_cvt_pk_bf16_f32 v65, v80, v81
	ds_read_b64_tr_b16 v[66:67], v202 offset:0
	ds_read_b64_tr_b16 v[68:69], v202 offset:0x400
	ds_read_b64_tr_b16 v[70:71], v202 offset:0x800
	s_waitcnt lgkmcnt(6)
	v_mfma_f32_32x32x16_bf16 v[98:113], v[228:231], v[146:149], v[98:113]
	ds_read_b64_tr_b16 v[72:73], v202 offset:0xc00
	ds_read_b64_tr_b16 v[74:75], v202 offset:0x1000
	ds_read_b64_tr_b16 v[76:77], v202 offset:0x1400
	ds_read_b64_tr_b16 v[78:79], v202 offset:0x1800
	ds_read_b64_tr_b16 v[80:81], v202 offset:0x1c00
	v_add_f32_e64 v124, v126, v124
	v_add_f32_e64 v125, v127, v125
	s_waitcnt lgkmcnt(10)
	v_mfma_f32_32x32x16_bf16 v[82:97], v[232:235], v[146:149], v[82:97]
	v_add_f32_e32 v124, v124, v125

; DEVI void finishSM(f32x16& p0, f32x16& p1, float alpha, float& l_reg, bf16x8& pa0, bf16x8& pa1, bf16x8& pa2, bf16x8& pa3) {
;     ...
;     float ps = s2[0] + s2[1];
;     { auto rr = __builtin_amdgcn_permlane32_swap(__float_as_uint(ps), __float_as_uint(ps), false, false);
;       ps = __uint_as_float(rr[0]) + __uint_as_float(rr[1]); }
	v_mov_b32_e32 v125, v124


; template <int OFF> DEVI s16x4 tr_read(int vb) { s16x4 r; asm volatile("ds_read_b64_tr_b16 %0, %1 offset:%2" : "=&v"(r) : "v"(vb), "i"(OFF) : "memory"); return r; }
; #define SBAR() __builtin_amdgcn_sched_barrier(0)
; DEVI void pv_both(f32x16& o0, f32x16& o1, int vb, bf16x8 pa0, bf16x8 pa1, bf16x8 pa2, bf16x8 pa3) {
;     const s16x4 a0 = tr_read<v_rd_off(0, 0, 0)>(vb), b0 = tr_read<v_rd_off(0, 0, 1)>(vb), a1 = tr_read<v_rd_off(0, 1, 0)>(vb), b1 = tr_read<v_rd_off(0, 1, 1)>(vb);
;     const s16x4 a2 = tr_read<v_rd_off(0, 2, 0)>(vb), b2 = tr_read<v_rd_off(0, 2, 1)>(vb), a3 = tr_read<v_rd_off(0, 3, 0)>(vb), b3 = tr_read<v_rd_off(0, 3, 1)>(vb);
;     const s16x4 c0 = tr_read<v_rd_off(1, 0, 0)>(vb), d0 = tr_read<v_rd_off(1, 0, 1)>(vb), c1 = tr_read<v_rd_off(1, 1, 0)>(vb), d1 = tr_read<v_rd_off(1, 1, 1)>(vb);
;     const s16x4 c2 = tr_read<v_rd_off(1, 2, 0)>(vb), d2 = tr_read<v_rd_off(1, 2, 1)>(vb), c3 = tr_read<v_rd_off(1, 3, 0)>(vb), d3 = tr_read<v_rd_off(1, 3, 1)>(vb);
;     asm volatile("s_waitcnt lgkmcnt(8)" ::: "memory"); SBAR();
;     ...
;     o0 = __builtin_amdgcn_mfma_f32_32x32x16_bf16(pa0, PK(a0, b0), o0, 0, 0, 0);
;     o0 = __builtin_amdgcn_mfma_f32_32x32x16_bf16(pa1, PK(a1, b1), o0, 0, 0, 0);
;     o0 = __builtin_amdgcn_mfma_f32_32x32x16_bf16(pa2, PK(a2, b2), o0, 0, 0, 0);
;     o0 = __builtin_amdgcn_mfma_f32_32x32x16_bf16(pa3, PK(a3, b3), o0, 0, 0, 0);
;     asm volatile("s_waitcnt lgkmcnt(0)" ::: "memory"); SBAR();
;     o1 = __builtin_amdgcn_mfma_f32_32x32x16_bf16(pa0, PK(c0, d0), o1, 0, 0, 0);
;     o1 = __builtin_amdgcn_mfma_f32_32x32x16_bf16(pa1, PK(c1, d1), o1, 0, 0, 0);
;     o1 = __builtin_amdgcn_mfma_f32_32x32x16_bf16(pa2, PK(c2, d2), o1, 0, 0, 0);
;     o1 = __builtin_amdgcn_mfma_f32_32x32x16_bf16(pa3, PK(c3, d3), o1, 0, 0, 0);
;     ...
; }
; template <bool FIRST> DEVI bool partialSM(f32x16& p0, f32x16& p1, float& m_reg, float& alpha) {
;     float pmax = p0[0];
; #pragma unroll
;     for (int r = 1; r < 16; ++r) pmax = fmaxf(pmax, p0[r]);
; #pragma unroll
;     for (int r = 0; r < 16; ++r) pmax = fmaxf(pmax, p1[r]);
;     { auto rr = __builtin_amdgcn_permlane32_swap(__float_as_uint(pmax), __float_as_uint(pmax), false, false);
;       pmax = fmaxf(__uint_as_float(rr[0]), __uint_as_float(rr[1])); }
	s_waitcnt lgkmcnt(9)
	v_mfma_f32_32x32x16_bf16 v[98:113], v[208:211], v[142:145], v[98:113]
	v_permlane32_swap_b32_e32 v124, v125
	ds_read_b64_tr_b16 v[208:209], v202 offset:0x200
	ds_read_b64_tr_b16 v[210:211], v202 offset:0x600
	ds_read_b64_tr_b16 v[212:213], v202 offset:0xa00
	ds_read_b64_tr_b16 v[214:215], v202 offset:0xe00
	ds_read_b64_tr_b16 v[216:217], v202 offset:0x1200
	ds_read_b64_tr_b16 v[218:219], v202 offset:0x1600
	ds_read_b64_tr_b16 v[220:221], v202 offset:0x1a00
	s_waitcnt lgkmcnt(15)
	v_mfma_f32_32x32x16_bf16 v[82:97], v[236:239], v[142:145], v[82:97]
	ds_read_b64_tr_b16 v[222:223], v202 offset:0x1e00
	s_waitcnt lgkmcnt(14)
	v_mfma_f32_32x32x16_bf16 v[18:33], v[50:53], v[66:69], v[18:33]
	s_waitcnt lgkmcnt(6)
	v_mfma_f32_32x32x16_bf16 v[2:17], v[50:53], v[208:211], v[2:17]
	s_nop 1
	v_max_f32_e32 v249, v99, v99
	v_max_f32_e32 v250, v98, v98
	v_max_f32_e32 v249, v250, v249
	v_max3_f32 v249, v249, v100, v101
	v_max3_f32 v249, v249, v102, v103
	v_max3_f32 v251, v249, v104, v105
	v_max3_f32 v251, v251, v106, v107
	v_exp_f32_e32 v50, v98
	v_exp_f32_e32 v51, v99
	v_exp_f32_e32 v52, v100
	v_exp_f32_e32 v53, v101
	v_mfma_f32_32x32x16_bf16 v[18:33], v[54:57], v[70:73], v[18:33]
	s_waitcnt lgkmcnt(4)
	v_mfma_f32_32x32x16_bf16 v[2:17], v[54:57], v[212:215], v[2:17]
	v_max3_f32 v251, v251, v108, v109
	v_max3_f32 v251, v251, v110, v111
	v_max3_f32 v251, v251, v112, v113
	v_max3_f32 v251, v251, v82, v83
	v_max3_f32 v251, v251, v84, v85
	v_max3_f32 v251, v251, v86, v87
	v_max3_f32 v251, v251, v88, v89
	v_exp_f32_e32 v54, v102
	v_exp_f32_e32 v55, v103
	v_exp_f32_e32 v56, v104
	v_exp_f32_e32 v57, v105
	v_mfma_f32_32x32x16_bf16 v[18:33], v[58:61], v[74:77], v[18:33]
	s_waitcnt lgkmcnt(2)
	v_mfma_f32_32x32x16_bf16 v[2:17], v[58:61], v[216:219], v[2:17]
	v_max3_f32 v251, v251, v90, v91
	v_max3_f32 v251, v251, v92, v93
	v_max3_f32 v251, v251, v94, v95
	v_max3_f32 v251, v251, v96, v97
	v_mov_b32_e32 v252, v251


; template <bool FIRST> DEVI bool partialSM(f32x16& p0, f32x16& p1, float& m_reg, float& alpha) {
;     float pmax = p0[0];
; #pragma unroll
;     for (int r = 1; r < 16; ++r) pmax = fmaxf(pmax, p0[r]);
; #pragma unroll
;     for (int r = 0; r < 16; ++r) pmax = fmaxf(pmax, p1[r]);
;     { auto rr = __builtin_amdgcn_permlane32_swap(__float_as_uint(pmax), __float_as_uint(pmax), false, false);
;       pmax = fmaxf(__uint_as_float(rr[0]), __uint_as_float(rr[1])); }
;     if (FIRST) { m_reg = pmax; alpha = 1.f;
; #pragma unroll
;         for (int r = 0; r < 16; ++r) { p0[r] = __builtin_amdgcn_exp2f(p0[r] - pmax); p1[r] = p1[r] - pmax; }
;         return false;
;     } else if (__builtin_expect(__all(pmax <= ATT_THR), 1)) { alpha = 1.f;
; #pragma unroll
;         for (int r = 0; r < 16; ++r) p0[r] = __builtin_amdgcn_exp2f(p0[r]);
;         return false;
	v_exp_f32_e32 v58, v106
	v_exp_f32_e32 v59, v107
	v_permlane32_swap_b32_e32 v251, v252
	v_exp_f32_e32 v60, v108
	v_exp_f32_e32 v61, v109
	v_mfma_f32_32x32x16_bf16 v[18:33], v[62:65], v[78:81], v[18:33]
	s_waitcnt lgkmcnt(0)
	v_mfma_f32_32x32x16_bf16 v[2:17], v[62:65], v[220:223], v[2:17]
	v_exp_f32_e32 v62, v110
	v_exp_f32_e32 v63, v111
	v_exp_f32_e32 v64, v112
	v_exp_f32_e32 v65, v113
	v_max_f32_e32 v252, v252, v252
	v_max_f32_e32 v251, v251, v251
	v_max_f32_e32 v126, v251, v252
	v_cmp_ge_f32_e32 vcc, s79, v126
	s_cmp_lg_u64 vcc, exec
	s_cselect_b64 s[6:7], -1, 0
	s_cbranch_scc1 .LBB0_705
	v_mov_b32_e32 v208, 1.0
	v_mov_b32_e32 v209, v203
	v_exp_f32_e32 v82, v82
	v_exp_f32_e32 v83, v83
	v_exp_f32_e32 v84, v84
	v_exp_f32_e32 v85, v85
	v_exp_f32_e32 v86, v86
	v_exp_f32_e32 v87, v87
	v_exp_f32_e32 v88, v88
	v_exp_f32_e32 v89, v89
	v_exp_f32_e32 v90, v90
	v_exp_f32_e32 v91, v91
	v_exp_f32_e32 v92, v92
	v_exp_f32_e32 v93, v93
	v_exp_f32_e32 v94, v94
	v_exp_f32_e32 v95, v95
	v_exp_f32_e32 v96, v96
	v_exp_f32_e32 v97, v97
	s_branch .LBB0_699

; #define PK4(P, BASE, OUT) do { u32x4 w = {cvt_pk_bf16(P[BASE + 0], P[BASE + 1]), cvt_pk_bf16(P[BASE + 2], P[BASE + 3]), cvt_pk_bf16(P[BASE + 4], P[BASE + 5]), cvt_pk_bf16(P[BASE + 6], P[BASE + 7])}; \
;     OUT = *reinterpret_cast<bf16x8*>(&w); } while (0)
; #define B_RESC(a, rare) do { if (rare) { if (hi == 0) al_l[r32] = (a); asm volatile("s_waitcnt lgkmcnt(0)" ::: "memory"); __builtin_amdgcn_wave_barrier(); \
;         _Pragma("unroll") for (int _d = 0; _d < 2; ++_d) _Pragma("unroll") for (int _r = 0; _r < 16; ++_r) o[_d][_r] *= al_l[crow(_r, hi)]; C_SPLAT(); } } while (0)
; DEVI void finishSM(f32x16& p0, f32x16& p1, float alpha, float& l_reg, bf16x8& pa0, bf16x8& pa1, bf16x8& pa2, bf16x8& pa3) {
; #pragma unroll
;     for (int r = 0; r < 16; ++r) p1[r] = __builtin_amdgcn_exp2f(p1[r]);
;     f32x2 s2 = (f32x2){p0[0], p0[1]} + (f32x2){p1[0], p1[1]};
; #pragma unroll
;     for (int r = 2; r < 16; r += 2) s2 += (f32x2){p0[r], p0[r + 1]} + (f32x2){p1[r], p1[r + 1]};
;     float ps = s2[0] + s2[1];
;     { auto rr = __builtin_amdgcn_permlane32_swap(__float_as_uint(ps), __float_as_uint(ps), false, false);
;       ps = __uint_as_float(rr[0]) + __uint_as_float(rr[1]); }
;     l_reg = l_reg * alpha + ps;
;     ...
;     PK4(p0, 0, pa0); PK4(p0, 8, pa1); PK4(p1, 0, pa2); PK4(p1, 8, pa3);
;     ...
; }
; DEVI void qkt(f32x16& p0, f32x16& p1, const char* Kb, const bf16x8 (&qr)[6], int r32, int hi, const f32x16& cinit) {
; #pragma unroll
;     for (int d0 = 0; d0 < 6; ++d0) { const int cb = (d0 * 16 + hi * 8) * 2;
;         const bf16x8 k0 = *(const bf16x8*)(Kb + KSWZ(r32, cb)), k1 = *(const bf16x8*)(Kb + KSWZ(32 + r32, cb));
;         p0 = __builtin_amdgcn_mfma_f32_32x32x16_bf16(k0, qr[d0], d0 == 0 ? cinit : p0, 0, 0, 0);
;         p1 = __builtin_amdgcn_mfma_f32_32x32x16_bf16(k1, qr[d0], d0 == 0 ? cinit : p1, 0, 0, 0); }
; }
; DEVI void attn_unit8(const Params& p, char* smem, int unit, int l, int& cvs  , CvRun& crun) {
;     ...
;         __syncthreads();
;         if (T + 2 < NTILE) B_DMA(T + 2, s2);
;         qkt(pA0, pA1, K_lds + s1 * 24576, qr, r32, hi, cinit);
;         finishSM(pB0, pB1, alB, l_reg, pa0, pa1, pa2, pa3);
;         pv_both(o[0], o[1], vb + 8192, pa0, pa1, pa2, pa3);
;         { const bool rr_ = partialSM<false>(pA0, pA1, m_reg, alA); B_RESC(alA, rr_); }
.LBB0_702:
	s_mul_i32 s98, s2, 0x6000
	s_add_i32 s98, s96, s98
	s_lshl_b32 s99, s2, 14
	s_add_i32 s99, s97, s99
	s_mul_i32 s6, s61, 0x6000
	s_add_i32 s6, s6, 0
	v_add_u32_e32 v249, s6, v129
	v_lshl_add_u64 v[250:251], v[118:119], 0, s[12:13]
	s_mov_b32 m0, s98
	s_barrier
	ds_read_b128 v[234:237], v249
	ds_read_b128 v[210:213], v249 offset:6144
	global_load_lds_dwordx4 v[250:251], off
	s_waitcnt lgkmcnt(1)
	v_mfma_f32_32x32x16_bf16 v[98:113], v[234:237], v[150:153], v[34:49]
	v_add_u32_e32 v126, s6, v184
	v_lshl_add_u64 v[250:251], v[120:121], 0, s[12:13]
	s_add_i32 m0, s98, 0x2000
	global_load_lds_dwordx4 v[250:251], off
	s_waitcnt lgkmcnt(0)
	v_mfma_f32_32x32x16_bf16 v[66:81], v[210:213], v[150:153], v[34:49]
	ds_read_b128 v[210:213], v126
	ds_read_b128 v[214:217], v126 offset:6144
	v_add_u32_e32 v126, s6, v185
	v_lshl_add_u64 v[250:251], v[122:123], 0, s[12:13]
	s_add_i32 m0, s98, 0x4000
	global_load_lds_dwordx4 v[250:251], off
	s_waitcnt lgkmcnt(1)
	v_mfma_f32_32x32x16_bf16 v[98:113], v[210:213], v[138:141], v[98:113]
	s_mov_b32 m0, s99
	v_lshl_add_u64 v[250:251], v[116:117], 0, s[40:41]
	global_load_lds_dwordx4 v[116:117], off
	s_add_i32 m0, s99, 0x2000
	v_add_u32_e32 v174, 0x2000, v202
	global_load_lds_dwordx4 v[250:251], off
	s_waitcnt lgkmcnt(0)
	v_mfma_f32_32x32x16_bf16 v[66:81], v[214:217], v[138:141], v[66:81]
	ds_read_b128 v[210:213], v126
	ds_read_b128 v[214:217], v126 offset:6144
	v_add_u32_e32 v126, s6, v204
	s_waitcnt lgkmcnt(1)
	v_mfma_f32_32x32x16_bf16 v[98:113], v[210:213], v[134:137], v[98:113]
	ds_read_b128 v[210:213], v126
	ds_read_b128 v[218:221], v126 offset:6144
	v_add_u32_e32 v126, s6, v205
	s_waitcnt lgkmcnt(2)
	v_mfma_f32_32x32x16_bf16 v[66:81], v[214:217], v[134:137], v[66:81]
	ds_read_b128 v[214:217], v126
	ds_read_b128 v[222:225], v126 offset:6144
	v_add_u32_e32 v126, s6, v206
	ds_read_b128 v[226:229], v126
	ds_read_b128 v[230:233], v126 offset:6144
	v_add_f32_e32 v126, v50, v82
	v_add_f32_e32 v127, v51, v83
	v_cvt_pk_bf16_f32 v50, v50, v51
	v_cvt_pk_bf16_f32 v51, v52, v53
	s_waitcnt lgkmcnt(5)
	v_mfma_f32_32x32x16_bf16 v[98:113], v[210:213], v[130:133], v[98:113]
	v_add_f32_e64 v210, v52, v84
	v_add_f32_e64 v211, v53, v85
	v_cvt_pk_bf16_f32 v52, v54, v55
	v_cvt_pk_bf16_f32 v53, v56, v57
	v_add_f32_e64 v126, v210, v126
	v_add_f32_e64 v127, v211, v127
	v_add_f32_e64 v210, v54, v86
	v_add_f32_e64 v211, v55, v87
	v_cvt_pk_bf16_f32 v54, v58, v59
	s_waitcnt lgkmcnt(4)
	v_mfma_f32_32x32x16_bf16 v[66:81], v[218:221], v[130:133], v[66:81]
	v_add_f32_e64 v126, v210, v126
	v_add_f32_e64 v127, v211, v127
	v_add_f32_e64 v210, v56, v88
	v_add_f32_e64 v211, v57, v89
	v_cvt_pk_bf16_f32 v55, v60, v61
	v_cvt_pk_bf16_f32 v56, v62, v63
	v_cvt_pk_bf16_f32 v57, v64, v65
	v_add_f32_e64 v126, v210, v126
	v_add_f32_e64 v127, v211, v127
	v_add_f32_e32 v210, v58, v90
	v_add_f32_e32 v211, v59, v91
	v_cvt_pk_bf16_f32 v58, v82, v83
	v_cvt_pk_bf16_f32 v59, v84, v85
	s_waitcnt lgkmcnt(3)
	v_mfma_f32_32x32x16_bf16 v[98:113], v[214:217], v[146:149], v[98:113]
	v_add_f32_e64 v126, v210, v126
	v_add_f32_e64 v127, v211, v127
	v_add_f32_e64 v210, v60, v92
	v_add_f32_e64 v211, v61, v93
	v_cvt_pk_bf16_f32 v60, v86, v87
	v_cvt_pk_bf16_f32 v61, v88, v89
	v_add_f32_e64 v126, v210, v126
	v_add_f32_e64 v127, v211, v127
	v_add_f32_e32 v210, v62, v94
	v_add_f32_e32 v211, v63, v95
	v_cvt_pk_bf16_f32 v62, v90, v91
	v_cvt_pk_bf16_f32 v63, v92, v93
	s_waitcnt lgkmcnt(2)
	v_mfma_f32_32x32x16_bf16 v[66:81], v[222:225], v[146:149], v[66:81]
	v_add_f32_e64 v126, v210, v126
	v_add_f32_e64 v127, v211, v127
	v_add_f32_e64 v210, v64, v96
	v_add_f32_e64 v211, v65, v97
	v_cvt_pk_bf16_f32 v64, v94, v95
	v_cvt_pk_bf16_f32 v65, v96, v97
	ds_read_b64_tr_b16 v[154:155], v174 offset:0
	ds_read_b64_tr_b16 v[156:157], v174 offset:0x400
	ds_read_b64_tr_b16 v[158:159], v174 offset:0x800
	ds_read_b64_tr_b16 v[160:161], v174 offset:0xc00
	ds_read_b64_tr_b16 v[162:163], v174 offset:0x1000
	ds_read_b64_tr_b16 v[164:165], v174 offset:0x1400
	ds_read_b64_tr_b16 v[166:167], v174 offset:0x1800
	ds_read_b64_tr_b16 v[168:169], v174 offset:0x1c00
	v_add_f32_e64 v126, v210, v126
	v_add_f32_e64 v127, v211, v127
	ds_read_b64_tr_b16 v[210:211], v174 offset:0x200
	ds_read_b64_tr_b16 v[212:213], v174 offset:0x600
	ds_read_b64_tr_b16 v[214:215], v174 offset:0xa00
	s_waitcnt lgkmcnt(12)
	v_mfma_f32_32x32x16_bf16 v[98:113], v[226:229], v[142:145], v[98:113]
	ds_read_b64_tr_b16 v[216:217], v174 offset:0xe00
	ds_read_b64_tr_b16 v[218:219], v174 offset:0x1200
	ds_read_b64_tr_b16 v[220:221], v174 offset:0x1600
	ds_read_b64_tr_b16 v[222:223], v174 offset:0x1a00
	ds_read_b64_tr_b16 v[224:225], v174 offset:0x1e00
	v_add_f32_e32 v126, v126, v127
	s_waitcnt lgkmcnt(15)
	v_mfma_f32_32x32x16_bf16 v[66:81], v[230:233], v[142:145], v[66:81]
	v_mov_b32_e32 v127, v126


; template <int OFF> DEVI s16x4 tr_read(int vb) { s16x4 r; asm volatile("ds_read_b64_tr_b16 %0, %1 offset:%2" : "=&v"(r) : "v"(vb), "i"(OFF) : "memory"); return r; }
; #define SBAR() __builtin_amdgcn_sched_barrier(0)
; DEVI void pv_both(f32x16& o0, f32x16& o1, int vb, bf16x8 pa0, bf16x8 pa1, bf16x8 pa2, bf16x8 pa3) {
;     const s16x4 a0 = tr_read<v_rd_off(0, 0, 0)>(vb), b0 = tr_read<v_rd_off(0, 0, 1)>(vb), a1 = tr_read<v_rd_off(0, 1, 0)>(vb), b1 = tr_read<v_rd_off(0, 1, 1)>(vb);
;     const s16x4 a2 = tr_read<v_rd_off(0, 2, 0)>(vb), b2 = tr_read<v_rd_off(0, 2, 1)>(vb), a3 = tr_read<v_rd_off(0, 3, 0)>(vb), b3 = tr_read<v_rd_off(0, 3, 1)>(vb);
;     const s16x4 c0 = tr_read<v_rd_off(1, 0, 0)>(vb), d0 = tr_read<v_rd_off(1, 0, 1)>(vb), c1 = tr_read<v_rd_off(1, 1, 0)>(vb), d1 = tr_read<v_rd_off(1, 1, 1)>(vb);
;     const s16x4 c2 = tr_read<v_rd_off(1, 2, 0)>(vb), d2 = tr_read<v_rd_off(1, 2, 1)>(vb), c3 = tr_read<v_rd_off(1, 3, 0)>(vb), d3 = tr_read<v_rd_off(1, 3, 1)>(vb);
;     asm volatile("s_waitcnt lgkmcnt(8)" ::: "memory"); SBAR();
;     ...
;     o0 = __builtin_amdgcn_mfma_f32_32x32x16_bf16(pa0, PK(a0, b0), o0, 0, 0, 0);
;     o0 = __builtin_amdgcn_mfma_f32_32x32x16_bf16(pa1, PK(a1, b1), o0, 0, 0, 0);
;     o0 = __builtin_amdgcn_mfma_f32_32x32x16_bf16(pa2, PK(a2, b2), o0, 0, 0, 0);
;     o0 = __builtin_amdgcn_mfma_f32_32x32x16_bf16(pa3, PK(a3, b3), o0, 0, 0, 0);
;     asm volatile("s_waitcnt lgkmcnt(0)" ::: "memory"); SBAR();
;     o1 = __builtin_amdgcn_mfma_f32_32x32x16_bf16(pa0, PK(c0, d0), o1, 0, 0, 0);
;     o1 = __builtin_amdgcn_mfma_f32_32x32x16_bf16(pa1, PK(c1, d1), o1, 0, 0, 0);
;     o1 = __builtin_amdgcn_mfma_f32_32x32x16_bf16(pa2, PK(c2, d2), o1, 0, 0, 0);
;     o1 = __builtin_amdgcn_mfma_f32_32x32x16_bf16(pa3, PK(c3, d3), o1, 0, 0, 0);
;     ...
; }
; template <bool FIRST> DEVI bool partialSM(f32x16& p0, f32x16& p1, float& m_reg, float& alpha) {
;     float pmax = p0[0];
; #pragma unroll
;     for (int r = 1; r < 16; ++r) pmax = fmaxf(pmax, p0[r]);
; #pragma unroll
;     for (int r = 0; r < 16; ++r) pmax = fmaxf(pmax, p1[r]);
;     { auto rr = __builtin_amdgcn_permlane32_swap(__float_as_uint(pmax), __float_as_uint(pmax), false, false);
;       pmax = fmaxf(__uint_as_float(rr[0]), __uint_as_float(rr[1])); }
	s_waitcnt lgkmcnt(14)
	v_mfma_f32_32x32x16_bf16 v[18:33], v[50:53], v[154:157], v[18:33]
	v_permlane32_swap_b32_e32 v126, v127
	s_waitcnt lgkmcnt(6)
	v_mfma_f32_32x32x16_bf16 v[2:17], v[50:53], v[210:213], v[2:17]
	s_nop 1
	v_max_f32_e32 v249, v99, v99
	v_max_f32_e32 v250, v98, v98
	v_max_f32_e32 v249, v250, v249
	v_max3_f32 v249, v249, v100, v101
	v_max3_f32 v249, v249, v102, v103
	v_max3_f32 v251, v249, v104, v105
	v_max3_f32 v251, v251, v106, v107
	v_exp_f32_e32 v50, v98
	v_exp_f32_e32 v51, v99
	v_exp_f32_e32 v52, v100
	v_exp_f32_e32 v53, v101
	v_mfma_f32_32x32x16_bf16 v[18:33], v[54:57], v[158:161], v[18:33]
	s_waitcnt lgkmcnt(4)
	v_mfma_f32_32x32x16_bf16 v[2:17], v[54:57], v[214:217], v[2:17]
	v_max3_f32 v251, v251, v108, v109
	v_max3_f32 v251, v251, v110, v111
	v_max3_f32 v251, v251, v112, v113
	v_max3_f32 v251, v251, v66, v67
	v_max3_f32 v251, v251, v68, v69
	v_max3_f32 v251, v251, v70, v71
	v_max3_f32 v251, v251, v72, v73
	v_exp_f32_e32 v54, v102
	v_exp_f32_e32 v55, v103
	v_exp_f32_e32 v56, v104
	v_exp_f32_e32 v57, v105
	v_mfma_f32_32x32x16_bf16 v[18:33], v[58:61], v[162:165], v[18:33]
	s_waitcnt lgkmcnt(2)
	v_mfma_f32_32x32x16_bf16 v[2:17], v[58:61], v[218:221], v[2:17]
	v_max3_f32 v251, v251, v74, v75
	v_max3_f32 v251, v251, v76, v77
	v_max3_f32 v251, v251, v78, v79
	v_max3_f32 v251, v251, v80, v81
	v_mov_b32_e32 v252, v251


; template <bool FIRST> DEVI bool partialSM(f32x16& p0, f32x16& p1, float& m_reg, float& alpha) {
;     float pmax = p0[0];
; #pragma unroll
;     for (int r = 1; r < 16; ++r) pmax = fmaxf(pmax, p0[r]);
; #pragma unroll
;     for (int r = 0; r < 16; ++r) pmax = fmaxf(pmax, p1[r]);
;     { auto rr = __builtin_amdgcn_permlane32_swap(__float_as_uint(pmax), __float_as_uint(pmax), false, false);
;       pmax = fmaxf(__uint_as_float(rr[0]), __uint_as_float(rr[1])); }
;     if (FIRST) { m_reg = pmax; alpha = 1.f;
; #pragma unroll
;         for (int r = 0; r < 16; ++r) { p0[r] = __builtin_amdgcn_exp2f(p0[r] - pmax); p1[r] = p1[r] - pmax; }
;         return false;
;     } else if (__builtin_expect(__all(pmax <= ATT_THR), 1)) { alpha = 1.f;
; #pragma unroll
;         for (int r = 0; r < 16; ++r) p0[r] = __builtin_amdgcn_exp2f(p0[r]);
;         return false;
	v_exp_f32_e32 v58, v106
	v_exp_f32_e32 v59, v107
	v_permlane32_swap_b32_e32 v251, v252
	v_exp_f32_e32 v60, v108
	v_exp_f32_e32 v61, v109
	v_mfma_f32_32x32x16_bf16 v[18:33], v[62:65], v[166:169], v[18:33]
	s_waitcnt lgkmcnt(0)
	v_mfma_f32_32x32x16_bf16 v[2:17], v[62:65], v[222:225], v[2:17]
	v_exp_f32_e32 v62, v110
	v_exp_f32_e32 v63, v111
	v_exp_f32_e32 v64, v112
	v_exp_f32_e32 v65, v113
	v_max_f32_e32 v252, v252, v252
	v_max_f32_e32 v251, v251, v251
	v_max_f32_e32 v174, v251, v252
	v_cmp_ge_f32_e32 vcc, s79, v174
	s_cmp_lg_u64 vcc, exec
	s_cselect_b64 s[6:7], -1, 0
	s_cbranch_scc1 .LBB0_711
	v_mov_b32_e32 v202, 1.0
	v_mov_b32_e32 v203, v209
	s_branch .LBB0_716

; template <bool FIRST> DEVI bool partialSM(f32x16& p0, f32x16& p1, float& m_reg, float& alpha) {
;     float pmax = p0[0];
; #pragma unroll
;     for (int r = 1; r < 16; ++r) pmax = fmaxf(pmax, p0[r]);
; #pragma unroll
;     for (int r = 0; r < 16; ++r) pmax = fmaxf(pmax, p1[r]);
;     { auto rr = __builtin_amdgcn_permlane32_swap(__float_as_uint(pmax), __float_as_uint(pmax), false, false);
;       pmax = fmaxf(__uint_as_float(rr[0]), __uint_as_float(rr[1])); }
;     if (FIRST) { m_reg = pmax; alpha = 1.f;
; #pragma unroll
;         for (int r = 0; r < 16; ++r) { p0[r] = __builtin_amdgcn_exp2f(p0[r] - pmax); p1[r] = p1[r] - pmax; }
;         return false;
;     } else if (__builtin_expect(__all(pmax <= ATT_THR), 1)) { alpha = 1.f;
; #pragma unroll
;         for (int r = 0; r < 16; ++r) p0[r] = __builtin_amdgcn_exp2f(p0[r]);
;         return false;
;     } else { const float d = fmaxf(pmax, 0.f); alpha = __builtin_amdgcn_exp2f(-d); m_reg += d;
; #pragma unroll
;         for (int r = 0; r < 16; ++r) { p0[r] = __builtin_amdgcn_exp2f(p0[r] - d); p1[r] = p1[r] - d; }
;         return true;
;     }
; }
; DEVI void finishSM(f32x16& p0, f32x16& p1, float alpha, float& l_reg, bf16x8& pa0, bf16x8& pa1, bf16x8& pa2, bf16x8& pa3) {
; #pragma unroll
;     for (int r = 0; r < 16; ++r) p1[r] = __builtin_amdgcn_exp2f(p1[r]);
;     f32x2 s2 = (f32x2){p0[0], p0[1]} + (f32x2){p1[0], p1[1]};
; #pragma unroll
;     for (int r = 2; r < 16; r += 2) s2 += (f32x2){p0[r], p0[r + 1]} + (f32x2){p1[r], p1[r + 1]};
;     float ps = s2[0] + s2[1];
;     { auto rr = __builtin_amdgcn_permlane32_swap(__float_as_uint(ps), __float_as_uint(ps), false, false);
;       ps = __uint_as_float(rr[0]) + __uint_as_float(rr[1]); }
;     l_reg = l_reg * alpha + ps;
;     ...
;     PK4(p0, 0, pa0); PK4(p0, 8, pa1); PK4(p1, 0, pa2); PK4(p1, 8, pa3);
;     ...
; }
; DEVI void qkt(f32x16& p0, f32x16& p1, const char* Kb, const bf16x8 (&qr)[6], int r32, int hi, const f32x16& cinit) {
; #pragma unroll
;     for (int d0 = 0; d0 < 6; ++d0) { const int cb = (d0 * 16 + hi * 8) * 2;
;         const bf16x8 k0 = *(const bf16x8*)(Kb + KSWZ(r32, cb)), k1 = *(const bf16x8*)(Kb + KSWZ(32 + r32, cb));
;         p0 = __builtin_amdgcn_mfma_f32_32x32x16_bf16(k0, qr[d0], d0 == 0 ? cinit : p0, 0, 0, 0);
;         p1 = __builtin_amdgcn_mfma_f32_32x32x16_bf16(k1, qr[d0], d0 == 0 ? cinit : p1, 0, 0, 0); }
; }
.LBB0_2260:
	v_add_u32_e32 v174, s98, v205
	v_exp_f32_e32 v66, v66
	v_exp_f32_e32 v67, v67
	s_waitcnt lgkmcnt(1)
	v_mfma_f32_32x32x16_bf16 v[98:113], v[82:85], v[150:153], v[34:49]
	v_add_u32_e32 v82, s98, v184
	v_add_u32_e32 v83, s98, v185
	ds_read_b128 v[210:213], v82 offset:12288
	ds_read_b128 v[214:217], v82 offset:18432
	ds_read_b128 v[218:221], v83 offset:12288
	ds_read_b128 v[222:225], v83 offset:18432
	v_exp_f32_e32 v68, v68
	v_exp_f32_e32 v69, v69
	v_exp_f32_e32 v70, v70
	v_exp_f32_e32 v71, v71
	s_waitcnt lgkmcnt(4)
	v_mfma_f32_32x32x16_bf16 v[82:97], v[124:127], v[150:153], v[34:49]
	ds_read_b128 v[124:127], v174 offset:12288
	ds_read_b128 v[226:229], v174 offset:18432
	v_exp_f32_e32 v72, v72
	v_exp_f32_e32 v73, v73
	v_exp_f32_e32 v74, v74
	v_exp_f32_e32 v75, v75
	v_exp_f32_e32 v76, v76
	v_exp_f32_e32 v77, v77
	s_waitcnt lgkmcnt(5)
	v_mfma_f32_32x32x16_bf16 v[98:113], v[210:213], v[138:141], v[98:113]
	v_add_u32_e32 v174, s98, v206
	v_exp_f32_e32 v78, v78
	v_exp_f32_e32 v79, v79
	ds_read_b128 v[230:233], v174 offset:12288
	ds_read_b128 v[234:237], v174 offset:18432
	v_exp_f32_e32 v80, v80
	v_exp_f32_e32 v81, v81
	v_add_u32_e32 v174, s98, v207
	s_waitcnt lgkmcnt(6)
	v_mfma_f32_32x32x16_bf16 v[82:97], v[214:217], v[138:141], v[82:97]
	v_add_f32_e64 v214, v50, v66
	v_add_f32_e64 v215, v51, v67
	v_add_f32_e64 v216, v52, v68
	v_add_f32_e64 v217, v53, v69
	v_lshl_add_u32 v203, s71, 14, v115
	v_add_f32_e32 v214, v216, v214
	v_add_f32_e32 v215, v217, v215
	v_add_f32_e32 v216, v54, v70
	v_add_f32_e32 v217, v55, v71
	ds_read_b128 v[210:213], v174 offset:12288
	ds_read_b128 v[238:241], v174 offset:18432
	v_add_f32_e32 v214, v216, v214
	v_add_f32_e32 v215, v217, v215
	s_waitcnt lgkmcnt(7)
	v_mfma_f32_32x32x16_bf16 v[98:113], v[218:221], v[134:137], v[98:113]
	v_add_f32_e64 v216, v56, v72
	v_add_f32_e64 v217, v57, v73
	v_cvt_pk_bf16_f32 v50, v50, v51
	v_cvt_pk_bf16_f32 v51, v52, v53
	v_cvt_pk_bf16_f32 v52, v54, v55
	v_cvt_pk_bf16_f32 v53, v56, v57
	v_cvt_pk_bf16_f32 v54, v58, v59
	v_add_f32_e64 v214, v216, v214
	v_add_f32_e64 v215, v217, v215
	s_waitcnt lgkmcnt(6)
	v_mfma_f32_32x32x16_bf16 v[82:97], v[222:225], v[134:137], v[82:97]
	v_add_f32_e64 v216, v58, v74
	v_add_f32_e64 v217, v59, v75
	v_cvt_pk_bf16_f32 v55, v60, v61
	v_cvt_pk_bf16_f32 v56, v62, v63
	v_cvt_pk_bf16_f32 v57, v64, v65
	v_cvt_pk_bf16_f32 v58, v66, v67
	v_cvt_pk_bf16_f32 v59, v68, v69
	v_add_f32_e64 v214, v216, v214
	v_add_f32_e64 v215, v217, v215
	s_waitcnt lgkmcnt(5)
	v_mfma_f32_32x32x16_bf16 v[98:113], v[124:127], v[130:133], v[98:113]
	v_add_f32_e64 v216, v60, v76
	v_add_f32_e64 v217, v61, v77
	v_add_f32_e64 v126, v62, v78
	v_add_f32_e64 v127, v63, v79
	v_add_f32_e64 v124, v216, v214
	v_add_f32_e64 v125, v217, v215
	v_cvt_pk_bf16_f32 v60, v70, v71
	v_cvt_pk_bf16_f32 v61, v72, v73
	v_cvt_pk_bf16_f32 v62, v74, v75
	v_cvt_pk_bf16_f32 v63, v76, v77
	s_waitcnt lgkmcnt(4)
	v_mfma_f32_32x32x16_bf16 v[82:97], v[226:229], v[130:133], v[82:97]
	v_add_f32_e64 v124, v126, v124
	v_add_f32_e64 v125, v127, v125
	v_add_f32_e64 v126, v64, v80
	v_add_f32_e64 v127, v65, v81
	v_cvt_pk_bf16_f32 v64, v78, v79
	v_cvt_pk_bf16_f32 v65, v80, v81
	ds_read_b64_tr_b16 v[66:67], v203 offset:0
	ds_read_b64_tr_b16 v[68:69], v203 offset:0x400
	ds_read_b64_tr_b16 v[70:71], v203 offset:0x800
	s_waitcnt lgkmcnt(6)
	v_mfma_f32_32x32x16_bf16 v[98:113], v[230:233], v[146:149], v[98:113]
	ds_read_b64_tr_b16 v[72:73], v203 offset:0xc00
	ds_read_b64_tr_b16 v[74:75], v203 offset:0x1000
	ds_read_b64_tr_b16 v[76:77], v203 offset:0x1400
	ds_read_b64_tr_b16 v[78:79], v203 offset:0x1800
	ds_read_b64_tr_b16 v[80:81], v203 offset:0x1c00
	v_add_f32_e64 v124, v126, v124
	v_add_f32_e64 v125, v127, v125
	s_waitcnt lgkmcnt(10)
	v_mfma_f32_32x32x16_bf16 v[82:97], v[234:237], v[146:149], v[82:97]
	v_add_f32_e32 v124, v124, v125

; DEVI void finishSM(f32x16& p0, f32x16& p1, float alpha, float& l_reg, bf16x8& pa0, bf16x8& pa1, bf16x8& pa2, bf16x8& pa3) {
;     ...
;     float ps = s2[0] + s2[1];
;     { auto rr = __builtin_amdgcn_permlane32_swap(__float_as_uint(ps), __float_as_uint(ps), false, false);
;       ps = __uint_as_float(rr[0]) + __uint_as_float(rr[1]); }
	v_mov_b32_e32 v125, v124


; template <int OFF> DEVI s16x4 tr_read(int vb) { s16x4 r; asm volatile("ds_read_b64_tr_b16 %0, %1 offset:%2" : "=&v"(r) : "v"(vb), "i"(OFF) : "memory"); return r; }
; #define SBAR() __builtin_amdgcn_sched_barrier(0)
; DEVI void pv_both(f32x16& o0, f32x16& o1, int vb, bf16x8 pa0, bf16x8 pa1, bf16x8 pa2, bf16x8 pa3) {
;     const s16x4 a0 = tr_read<v_rd_off(0, 0, 0)>(vb), b0 = tr_read<v_rd_off(0, 0, 1)>(vb), a1 = tr_read<v_rd_off(0, 1, 0)>(vb), b1 = tr_read<v_rd_off(0, 1, 1)>(vb);
;     const s16x4 a2 = tr_read<v_rd_off(0, 2, 0)>(vb), b2 = tr_read<v_rd_off(0, 2, 1)>(vb), a3 = tr_read<v_rd_off(0, 3, 0)>(vb), b3 = tr_read<v_rd_off(0, 3, 1)>(vb);
;     const s16x4 c0 = tr_read<v_rd_off(1, 0, 0)>(vb), d0 = tr_read<v_rd_off(1, 0, 1)>(vb), c1 = tr_read<v_rd_off(1, 1, 0)>(vb), d1 = tr_read<v_rd_off(1, 1, 1)>(vb);
;     const s16x4 c2 = tr_read<v_rd_off(1, 2, 0)>(vb), d2 = tr_read<v_rd_off(1, 2, 1)>(vb), c3 = tr_read<v_rd_off(1, 3, 0)>(vb), d3 = tr_read<v_rd_off(1, 3, 1)>(vb);
;     asm volatile("s_waitcnt lgkmcnt(8)" ::: "memory"); SBAR();
;     ...
;     o0 = __builtin_amdgcn_mfma_f32_32x32x16_bf16(pa0, PK(a0, b0), o0, 0, 0, 0);
;     o0 = __builtin_amdgcn_mfma_f32_32x32x16_bf16(pa1, PK(a1, b1), o0, 0, 0, 0);
;     o0 = __builtin_amdgcn_mfma_f32_32x32x16_bf16(pa2, PK(a2, b2), o0, 0, 0, 0);
;     o0 = __builtin_amdgcn_mfma_f32_32x32x16_bf16(pa3, PK(a3, b3), o0, 0, 0, 0);
;     asm volatile("s_waitcnt lgkmcnt(0)" ::: "memory"); SBAR();
;     o1 = __builtin_amdgcn_mfma_f32_32x32x16_bf16(pa0, PK(c0, d0), o1, 0, 0, 0);
;     o1 = __builtin_amdgcn_mfma_f32_32x32x16_bf16(pa1, PK(c1, d1), o1, 0, 0, 0);
;     o1 = __builtin_amdgcn_mfma_f32_32x32x16_bf16(pa2, PK(c2, d2), o1, 0, 0, 0);
;     o1 = __builtin_amdgcn_mfma_f32_32x32x16_bf16(pa3, PK(c3, d3), o1, 0, 0, 0);
;     ...
; }
; template <bool FIRST> DEVI bool partialSM(f32x16& p0, f32x16& p1, float& m_reg, float& alpha) {
;     float pmax = p0[0];
; #pragma unroll
;     for (int r = 1; r < 16; ++r) pmax = fmaxf(pmax, p0[r]);
; #pragma unroll
;     for (int r = 0; r < 16; ++r) pmax = fmaxf(pmax, p1[r]);
;     { auto rr = __builtin_amdgcn_permlane32_swap(__float_as_uint(pmax), __float_as_uint(pmax), false, false);
;       pmax = fmaxf(__uint_as_float(rr[0]), __uint_as_float(rr[1])); }
	s_waitcnt lgkmcnt(9)
	v_mfma_f32_32x32x16_bf16 v[98:113], v[210:213], v[142:145], v[98:113]
	v_permlane32_swap_b32_e32 v124, v125
	ds_read_b64_tr_b16 v[210:211], v203 offset:0x200
	ds_read_b64_tr_b16 v[212:213], v203 offset:0x600
	ds_read_b64_tr_b16 v[214:215], v203 offset:0xa00
	ds_read_b64_tr_b16 v[216:217], v203 offset:0xe00
	ds_read_b64_tr_b16 v[218:219], v203 offset:0x1200
	ds_read_b64_tr_b16 v[220:221], v203 offset:0x1600
	ds_read_b64_tr_b16 v[222:223], v203 offset:0x1a00
	s_waitcnt lgkmcnt(15)
	v_mfma_f32_32x32x16_bf16 v[82:97], v[238:241], v[142:145], v[82:97]
	ds_read_b64_tr_b16 v[224:225], v203 offset:0x1e00
	s_waitcnt lgkmcnt(14)
	v_mfma_f32_32x32x16_bf16 v[18:33], v[50:53], v[66:69], v[18:33]
	s_waitcnt lgkmcnt(6)
	v_mfma_f32_32x32x16_bf16 v[2:17], v[50:53], v[210:213], v[2:17]
	s_nop 1
	v_max_f32_e32 v249, v99, v99
	v_max_f32_e32 v250, v98, v98
	v_max_f32_e32 v249, v250, v249
	v_max3_f32 v249, v249, v100, v101
	v_max3_f32 v249, v249, v102, v103
	v_max3_f32 v251, v249, v104, v105
	v_max3_f32 v251, v251, v106, v107
	v_exp_f32_e32 v50, v98
	v_exp_f32_e32 v51, v99
	v_exp_f32_e32 v52, v100
	v_exp_f32_e32 v53, v101
	v_mfma_f32_32x32x16_bf16 v[18:33], v[54:57], v[70:73], v[18:33]
	s_waitcnt lgkmcnt(4)
	v_mfma_f32_32x32x16_bf16 v[2:17], v[54:57], v[214:217], v[2:17]
	v_max3_f32 v251, v251, v108, v109
	v_max3_f32 v251, v251, v110, v111
	v_max3_f32 v251, v251, v112, v113
	v_max3_f32 v251, v251, v82, v83
	v_max3_f32 v251, v251, v84, v85
	v_max3_f32 v251, v251, v86, v87
	v_max3_f32 v251, v251, v88, v89
	v_exp_f32_e32 v54, v102
	v_exp_f32_e32 v55, v103
	v_exp_f32_e32 v56, v104
	v_exp_f32_e32 v57, v105
	v_mfma_f32_32x32x16_bf16 v[18:33], v[58:61], v[74:77], v[18:33]
	s_waitcnt lgkmcnt(2)
	v_mfma_f32_32x32x16_bf16 v[2:17], v[58:61], v[218:221], v[2:17]
	v_max3_f32 v251, v251, v90, v91
	v_max3_f32 v251, v251, v92, v93
	v_max3_f32 v251, v251, v94, v95
	v_max3_f32 v251, v251, v96, v97
	v_mov_b32_e32 v252, v251


; template <bool FIRST> DEVI bool partialSM(f32x16& p0, f32x16& p1, float& m_reg, float& alpha) {
;     float pmax = p0[0];
; #pragma unroll
;     for (int r = 1; r < 16; ++r) pmax = fmaxf(pmax, p0[r]);
; #pragma unroll
;     for (int r = 0; r < 16; ++r) pmax = fmaxf(pmax, p1[r]);
;     { auto rr = __builtin_amdgcn_permlane32_swap(__float_as_uint(pmax), __float_as_uint(pmax), false, false);
;       pmax = fmaxf(__uint_as_float(rr[0]), __uint_as_float(rr[1])); }
;     if (FIRST) { m_reg = pmax; alpha = 1.f;
; #pragma unroll
;         for (int r = 0; r < 16; ++r) { p0[r] = __builtin_amdgcn_exp2f(p0[r] - pmax); p1[r] = p1[r] - pmax; }
;         return false;
;     } else if (__builtin_expect(__all(pmax <= ATT_THR), 1)) { alpha = 1.f;
; #pragma unroll
;         for (int r = 0; r < 16; ++r) p0[r] = __builtin_amdgcn_exp2f(p0[r]);
;         return false;
	v_exp_f32_e32 v58, v106
	v_exp_f32_e32 v59, v107
	v_permlane32_swap_b32_e32 v251, v252
	v_exp_f32_e32 v60, v108
	v_exp_f32_e32 v61, v109
	v_mfma_f32_32x32x16_bf16 v[18:33], v[62:65], v[78:81], v[18:33]
	s_waitcnt lgkmcnt(0)
	v_mfma_f32_32x32x16_bf16 v[2:17], v[62:65], v[222:225], v[2:17]
	v_exp_f32_e32 v62, v110
	v_exp_f32_e32 v63, v111
	v_exp_f32_e32 v64, v112
	v_exp_f32_e32 v65, v113
	v_max_f32_e32 v252, v252, v252
	v_max_f32_e32 v251, v251, v251
	v_max_f32_e32 v126, v251, v252
	v_cmp_ge_f32_e32 vcc, s80, v126
	s_cmp_lg_u64 vcc, exec
	s_cselect_b64 s[6:7], -1, 0
	s_cbranch_scc1 .LBB0_2269
	v_mov_b32_e32 v209, 1.0
	v_mov_b32_e32 v210, v204
	v_exp_f32_e32 v82, v82
	v_exp_f32_e32 v83, v83
	v_exp_f32_e32 v84, v84
	v_exp_f32_e32 v85, v85
	v_exp_f32_e32 v86, v86
	v_exp_f32_e32 v87, v87
	v_exp_f32_e32 v88, v88
	v_exp_f32_e32 v89, v89
	v_exp_f32_e32 v90, v90
	v_exp_f32_e32 v91, v91
	v_exp_f32_e32 v92, v92
	v_exp_f32_e32 v93, v93
	v_exp_f32_e32 v94, v94
	v_exp_f32_e32 v95, v95
	v_exp_f32_e32 v96, v96
	v_exp_f32_e32 v97, v97
	s_branch .LBB0_2263

; #define PK4(P, BASE, OUT) do { u32x4 w = {cvt_pk_bf16(P[BASE + 0], P[BASE + 1]), cvt_pk_bf16(P[BASE + 2], P[BASE + 3]), cvt_pk_bf16(P[BASE + 4], P[BASE + 5]), cvt_pk_bf16(P[BASE + 6], P[BASE + 7])}; \
;     OUT = *reinterpret_cast<bf16x8*>(&w); } while (0)
; #define B_RESC(a, rare) do { if (rare) { if (hi == 0) al_l[r32] = (a); asm volatile("s_waitcnt lgkmcnt(0)" ::: "memory"); __builtin_amdgcn_wave_barrier(); \
;         _Pragma("unroll") for (int _d = 0; _d < 2; ++_d) _Pragma("unroll") for (int _r = 0; _r < 16; ++_r) o[_d][_r] *= al_l[crow(_r, hi)]; C_SPLAT(); } } while (0)
; DEVI void finishSM(f32x16& p0, f32x16& p1, float alpha, float& l_reg, bf16x8& pa0, bf16x8& pa1, bf16x8& pa2, bf16x8& pa3) {
; #pragma unroll
;     for (int r = 0; r < 16; ++r) p1[r] = __builtin_amdgcn_exp2f(p1[r]);
;     f32x2 s2 = (f32x2){p0[0], p0[1]} + (f32x2){p1[0], p1[1]};
; #pragma unroll
;     for (int r = 2; r < 16; r += 2) s2 += (f32x2){p0[r], p0[r + 1]} + (f32x2){p1[r], p1[r + 1]};
;     float ps = s2[0] + s2[1];
;     { auto rr = __builtin_amdgcn_permlane32_swap(__float_as_uint(ps), __float_as_uint(ps), false, false);
;       ps = __uint_as_float(rr[0]) + __uint_as_float(rr[1]); }
;     l_reg = l_reg * alpha + ps;
;     ...
;     PK4(p0, 0, pa0); PK4(p0, 8, pa1); PK4(p1, 0, pa2); PK4(p1, 8, pa3);
;     ...
; }
; DEVI void qkt(f32x16& p0, f32x16& p1, const char* Kb, const bf16x8 (&qr)[6], int r32, int hi, const f32x16& cinit) {
; #pragma unroll
;     for (int d0 = 0; d0 < 6; ++d0) { const int cb = (d0 * 16 + hi * 8) * 2;
;         const bf16x8 k0 = *(const bf16x8*)(Kb + KSWZ(r32, cb)), k1 = *(const bf16x8*)(Kb + KSWZ(32 + r32, cb));
;         p0 = __builtin_amdgcn_mfma_f32_32x32x16_bf16(k0, qr[d0], d0 == 0 ? cinit : p0, 0, 0, 0);
;         p1 = __builtin_amdgcn_mfma_f32_32x32x16_bf16(k1, qr[d0], d0 == 0 ? cinit : p1, 0, 0, 0); }
; }
; DEVI void attn_unit8(const Params& p, char* smem, int unit, int l, int& cvs  , CvRun& crun) {
;     ...
;         __syncthreads();
;         if (T + 2 < NTILE) B_DMA(T + 2, s2);
;         qkt(pA0, pA1, K_lds + s1 * 24576, qr, r32, hi, cinit);
;         finishSM(pB0, pB1, alB, l_reg, pa0, pa1, pa2, pa3);
;         pv_both(o[0], o[1], vb + 8192, pa0, pa1, pa2, pa3);
;         { const bool rr_ = partialSM<false>(pA0, pA1, m_reg, alA); B_RESC(alA, rr_); }
.LBB0_2266:
	s_mul_i32 s98, s61, 0x6000
	s_add_i32 s98, s96, s98
	s_lshl_b32 s99, s61, 14
	s_add_i32 s99, s97, s99
	s_mul_i32 s6, s2, 0x6000
	s_add_i32 s6, s6, 0
	v_add_u32_e32 v249, s6, v129
	v_lshl_add_u64 v[250:251], v[118:119], 0, s[12:13]
	s_mov_b32 m0, s98
	s_barrier
	ds_read_b128 v[234:237], v249
	ds_read_b128 v[212:215], v249 offset:6144
	global_load_lds_dwordx4 v[250:251], off
	s_waitcnt lgkmcnt(1)
	v_mfma_f32_32x32x16_bf16 v[98:113], v[234:237], v[150:153], v[34:49]
	v_add_u32_e32 v126, s6, v184
	v_lshl_add_u64 v[250:251], v[120:121], 0, s[12:13]
	s_add_i32 m0, s98, 0x2000
	global_load_lds_dwordx4 v[250:251], off
	s_waitcnt lgkmcnt(0)
	v_mfma_f32_32x32x16_bf16 v[66:81], v[212:215], v[150:153], v[34:49]
	ds_read_b128 v[212:215], v126
	ds_read_b128 v[216:219], v126 offset:6144
	v_add_u32_e32 v126, s6, v185
	v_lshl_add_u64 v[250:251], v[122:123], 0, s[12:13]
	s_add_i32 m0, s98, 0x4000
	global_load_lds_dwordx4 v[250:251], off
	s_waitcnt lgkmcnt(1)
	v_mfma_f32_32x32x16_bf16 v[98:113], v[212:215], v[138:141], v[98:113]
	s_mov_b32 m0, s99
	v_lshl_add_u64 v[250:251], v[116:117], 0, s[40:41]
	global_load_lds_dwordx4 v[116:117], off
	s_add_i32 m0, s99, 0x2000
	v_add_u32_e32 v174, 0x2000, v203
	global_load_lds_dwordx4 v[250:251], off
	s_waitcnt lgkmcnt(0)
	v_mfma_f32_32x32x16_bf16 v[66:81], v[216:219], v[138:141], v[66:81]
	ds_read_b128 v[212:215], v126
	ds_read_b128 v[216:219], v126 offset:6144
	v_add_u32_e32 v126, s6, v205
	s_waitcnt lgkmcnt(1)
	v_mfma_f32_32x32x16_bf16 v[98:113], v[212:215], v[134:137], v[98:113]
	ds_read_b128 v[212:215], v126
	ds_read_b128 v[220:223], v126 offset:6144
	v_add_u32_e32 v126, s6, v206
	s_waitcnt lgkmcnt(2)
	v_mfma_f32_32x32x16_bf16 v[66:81], v[216:219], v[134:137], v[66:81]
	ds_read_b128 v[216:219], v126
	ds_read_b128 v[224:227], v126 offset:6144
	v_add_u32_e32 v126, s6, v207
	ds_read_b128 v[228:231], v126
	ds_read_b128 v[232:235], v126 offset:6144
	v_add_f32_e32 v126, v50, v82
	v_add_f32_e32 v127, v51, v83
	v_cvt_pk_bf16_f32 v50, v50, v51
	v_cvt_pk_bf16_f32 v51, v52, v53
	s_waitcnt lgkmcnt(5)
	v_mfma_f32_32x32x16_bf16 v[98:113], v[212:215], v[130:133], v[98:113]
	v_add_f32_e64 v212, v52, v84
	v_add_f32_e64 v213, v53, v85
	v_cvt_pk_bf16_f32 v52, v54, v55
	v_cvt_pk_bf16_f32 v53, v56, v57
	v_add_f32_e64 v126, v212, v126
	v_add_f32_e64 v127, v213, v127
	v_add_f32_e64 v212, v54, v86
	v_add_f32_e64 v213, v55, v87
	v_cvt_pk_bf16_f32 v54, v58, v59
	s_waitcnt lgkmcnt(4)
	v_mfma_f32_32x32x16_bf16 v[66:81], v[220:223], v[130:133], v[66:81]
	v_add_f32_e64 v126, v212, v126
	v_add_f32_e64 v127, v213, v127
	v_add_f32_e64 v212, v56, v88
	v_add_f32_e64 v213, v57, v89
	v_cvt_pk_bf16_f32 v55, v60, v61
	v_cvt_pk_bf16_f32 v56, v62, v63
	v_cvt_pk_bf16_f32 v57, v64, v65
	v_add_f32_e64 v126, v212, v126
	v_add_f32_e64 v127, v213, v127
	v_add_f32_e32 v212, v58, v90
	v_add_f32_e32 v213, v59, v91
	v_cvt_pk_bf16_f32 v58, v82, v83
	v_cvt_pk_bf16_f32 v59, v84, v85
	s_waitcnt lgkmcnt(3)
	v_mfma_f32_32x32x16_bf16 v[98:113], v[216:219], v[146:149], v[98:113]
	v_add_f32_e64 v126, v212, v126
	v_add_f32_e64 v127, v213, v127
	v_add_f32_e64 v212, v60, v92
	v_add_f32_e64 v213, v61, v93
	v_cvt_pk_bf16_f32 v60, v86, v87
	v_cvt_pk_bf16_f32 v61, v88, v89
	v_add_f32_e64 v126, v212, v126
	v_add_f32_e64 v127, v213, v127
	v_add_f32_e32 v212, v62, v94
	v_add_f32_e32 v213, v63, v95
	v_cvt_pk_bf16_f32 v62, v90, v91
	v_cvt_pk_bf16_f32 v63, v92, v93
	s_waitcnt lgkmcnt(2)
	v_mfma_f32_32x32x16_bf16 v[66:81], v[224:227], v[146:149], v[66:81]
	v_add_f32_e64 v126, v212, v126
	v_add_f32_e64 v127, v213, v127
	v_add_f32_e64 v212, v64, v96
	v_add_f32_e64 v213, v65, v97
	v_cvt_pk_bf16_f32 v64, v94, v95
	v_cvt_pk_bf16_f32 v65, v96, v97
	ds_read_b64_tr_b16 v[154:155], v174 offset:0
	ds_read_b64_tr_b16 v[156:157], v174 offset:0x400
	ds_read_b64_tr_b16 v[158:159], v174 offset:0x800
	ds_read_b64_tr_b16 v[160:161], v174 offset:0xc00
	ds_read_b64_tr_b16 v[162:163], v174 offset:0x1000
	ds_read_b64_tr_b16 v[164:165], v174 offset:0x1400
	ds_read_b64_tr_b16 v[166:167], v174 offset:0x1800
	ds_read_b64_tr_b16 v[168:169], v174 offset:0x1c00
	v_add_f32_e64 v126, v212, v126
	v_add_f32_e64 v127, v213, v127
	ds_read_b64_tr_b16 v[212:213], v174 offset:0x200
	ds_read_b64_tr_b16 v[214:215], v174 offset:0x600
	ds_read_b64_tr_b16 v[216:217], v174 offset:0xa00
	s_waitcnt lgkmcnt(12)
	v_mfma_f32_32x32x16_bf16 v[98:113], v[228:231], v[142:145], v[98:113]
	ds_read_b64_tr_b16 v[218:219], v174 offset:0xe00
	ds_read_b64_tr_b16 v[220:221], v174 offset:0x1200
	ds_read_b64_tr_b16 v[222:223], v174 offset:0x1600
	ds_read_b64_tr_b16 v[224:225], v174 offset:0x1a00
	ds_read_b64_tr_b16 v[226:227], v174 offset:0x1e00
	v_add_f32_e32 v126, v126, v127
	s_waitcnt lgkmcnt(15)
	v_mfma_f32_32x32x16_bf16 v[66:81], v[232:235], v[142:145], v[66:81]
	v_mov_b32_e32 v127, v126


; template <int OFF> DEVI s16x4 tr_read(int vb) { s16x4 r; asm volatile("ds_read_b64_tr_b16 %0, %1 offset:%2" : "=&v"(r) : "v"(vb), "i"(OFF) : "memory"); return r; }
; #define SBAR() __builtin_amdgcn_sched_barrier(0)
; DEVI void pv_both(f32x16& o0, f32x16& o1, int vb, bf16x8 pa0, bf16x8 pa1, bf16x8 pa2, bf16x8 pa3) {
;     const s16x4 a0 = tr_read<v_rd_off(0, 0, 0)>(vb), b0 = tr_read<v_rd_off(0, 0, 1)>(vb), a1 = tr_read<v_rd_off(0, 1, 0)>(vb), b1 = tr_read<v_rd_off(0, 1, 1)>(vb);
;     const s16x4 a2 = tr_read<v_rd_off(0, 2, 0)>(vb), b2 = tr_read<v_rd_off(0, 2, 1)>(vb), a3 = tr_read<v_rd_off(0, 3, 0)>(vb), b3 = tr_read<v_rd_off(0, 3, 1)>(vb);
;     const s16x4 c0 = tr_read<v_rd_off(1, 0, 0)>(vb), d0 = tr_read<v_rd_off(1, 0, 1)>(vb), c1 = tr_read<v_rd_off(1, 1, 0)>(vb), d1 = tr_read<v_rd_off(1, 1, 1)>(vb);
;     const s16x4 c2 = tr_read<v_rd_off(1, 2, 0)>(vb), d2 = tr_read<v_rd_off(1, 2, 1)>(vb), c3 = tr_read<v_rd_off(1, 3, 0)>(vb), d3 = tr_read<v_rd_off(1, 3, 1)>(vb);
;     asm volatile("s_waitcnt lgkmcnt(8)" ::: "memory"); SBAR();
;     ...
;     o0 = __builtin_amdgcn_mfma_f32_32x32x16_bf16(pa0, PK(a0, b0), o0, 0, 0, 0);
;     o0 = __builtin_amdgcn_mfma_f32_32x32x16_bf16(pa1, PK(a1, b1), o0, 0, 0, 0);
;     o0 = __builtin_amdgcn_mfma_f32_32x32x16_bf16(pa2, PK(a2, b2), o0, 0, 0, 0);
;     o0 = __builtin_amdgcn_mfma_f32_32x32x16_bf16(pa3, PK(a3, b3), o0, 0, 0, 0);
;     asm volatile("s_waitcnt lgkmcnt(0)" ::: "memory"); SBAR();
;     o1 = __builtin_amdgcn_mfma_f32_32x32x16_bf16(pa0, PK(c0, d0), o1, 0, 0, 0);
;     o1 = __builtin_amdgcn_mfma_f32_32x32x16_bf16(pa1, PK(c1, d1), o1, 0, 0, 0);
;     o1 = __builtin_amdgcn_mfma_f32_32x32x16_bf16(pa2, PK(c2, d2), o1, 0, 0, 0);
;     o1 = __builtin_amdgcn_mfma_f32_32x32x16_bf16(pa3, PK(c3, d3), o1, 0, 0, 0);
;     ...
; }
; template <bool FIRST> DEVI bool partialSM(f32x16& p0, f32x16& p1, float& m_reg, float& alpha) {
;     float pmax = p0[0];
; #pragma unroll
;     for (int r = 1; r < 16; ++r) pmax = fmaxf(pmax, p0[r]);
; #pragma unroll
;     for (int r = 0; r < 16; ++r) pmax = fmaxf(pmax, p1[r]);
;     { auto rr = __builtin_amdgcn_permlane32_swap(__float_as_uint(pmax), __float_as_uint(pmax), false, false);
;       pmax = fmaxf(__uint_as_float(rr[0]), __uint_as_float(rr[1])); }
	s_waitcnt lgkmcnt(14)
	v_mfma_f32_32x32x16_bf16 v[18:33], v[50:53], v[154:157], v[18:33]
	v_permlane32_swap_b32_e32 v126, v127
	s_waitcnt lgkmcnt(6)
	v_mfma_f32_32x32x16_bf16 v[2:17], v[50:53], v[212:215], v[2:17]
	s_nop 1
	v_max_f32_e32 v249, v99, v99
	v_max_f32_e32 v250, v98, v98
	v_max_f32_e32 v249, v250, v249
	v_max3_f32 v249, v249, v100, v101
	v_max3_f32 v249, v249, v102, v103
	v_max3_f32 v251, v249, v104, v105
	v_max3_f32 v251, v251, v106, v107
	v_exp_f32_e32 v50, v98
	v_exp_f32_e32 v51, v99
	v_exp_f32_e32 v52, v100
	v_exp_f32_e32 v53, v101
	v_mfma_f32_32x32x16_bf16 v[18:33], v[54:57], v[158:161], v[18:33]
	s_waitcnt lgkmcnt(4)
	v_mfma_f32_32x32x16_bf16 v[2:17], v[54:57], v[216:219], v[2:17]
	v_max3_f32 v251, v251, v108, v109
	v_max3_f32 v251, v251, v110, v111
	v_max3_f32 v251, v251, v112, v113
	v_max3_f32 v251, v251, v66, v67
	v_max3_f32 v251, v251, v68, v69
	v_max3_f32 v251, v251, v70, v71
	v_max3_f32 v251, v251, v72, v73
	v_exp_f32_e32 v54, v102
	v_exp_f32_e32 v55, v103
	v_exp_f32_e32 v56, v104
	v_exp_f32_e32 v57, v105
	v_mfma_f32_32x32x16_bf16 v[18:33], v[58:61], v[162:165], v[18:33]
	s_waitcnt lgkmcnt(2)
	v_mfma_f32_32x32x16_bf16 v[2:17], v[58:61], v[220:223], v[2:17]
	v_max3_f32 v251, v251, v74, v75
	v_max3_f32 v251, v251, v76, v77
	v_max3_f32 v251, v251, v78, v79
	v_max3_f32 v251, v251, v80, v81
	v_mov_b32_e32 v252, v251


; template <bool FIRST> DEVI bool partialSM(f32x16& p0, f32x16& p1, float& m_reg, float& alpha) {
;     float pmax = p0[0];
; #pragma unroll
;     for (int r = 1; r < 16; ++r) pmax = fmaxf(pmax, p0[r]);
; #pragma unroll
;     for (int r = 0; r < 16; ++r) pmax = fmaxf(pmax, p1[r]);
;     { auto rr = __builtin_amdgcn_permlane32_swap(__float_as_uint(pmax), __float_as_uint(pmax), false, false);
;       pmax = fmaxf(__uint_as_float(rr[0]), __uint_as_float(rr[1])); }
;     if (FIRST) { m_reg = pmax; alpha = 1.f;
; #pragma unroll
;         for (int r = 0; r < 16; ++r) { p0[r] = __builtin_amdgcn_exp2f(p0[r] - pmax); p1[r] = p1[r] - pmax; }
;         return false;
;     } else if (__builtin_expect(__all(pmax <= ATT_THR), 1)) { alpha = 1.f;
; #pragma unroll
;         for (int r = 0; r < 16; ++r) p0[r] = __builtin_amdgcn_exp2f(p0[r]);
;         return false;
	v_exp_f32_e32 v58, v106
	v_exp_f32_e32 v59, v107
	v_permlane32_swap_b32_e32 v251, v252
	v_exp_f32_e32 v60, v108
	v_exp_f32_e32 v61, v109
	v_mfma_f32_32x32x16_bf16 v[18:33], v[62:65], v[166:169], v[18:33]
	s_waitcnt lgkmcnt(0)
	v_mfma_f32_32x32x16_bf16 v[2:17], v[62:65], v[224:227], v[2:17]
	v_exp_f32_e32 v62, v110
	v_exp_f32_e32 v63, v111
	v_exp_f32_e32 v64, v112
	v_exp_f32_e32 v65, v113
	v_max_f32_e32 v252, v252, v252
	v_max_f32_e32 v251, v251, v251
	v_max_f32_e32 v174, v251, v252
	v_cmp_ge_f32_e32 vcc, s80, v174
	s_cmp_lg_u64 vcc, exec
	s_cselect_b64 s[6:7], -1, 0
	s_cbranch_scc1 .LBB0_2275
	v_mov_b32_e32 v203, 1.0
	v_mov_b32_e32 v204, v210
	s_branch .LBB0_2280
